# speedup vs baseline: 1.0334x; 1.0334x over previous
_Z12final_kernelPKDF16_S0_PKfS2_S2_S2_Pf:
	s_load_dwordx8 s[4:11], s[0:1], 0x0
	s_load_dwordx2 s[14:15], s[0:1], 0x20
	s_load_dwordx4 s[16:19], s[0:1], 0x28
	v_readfirstlane_b32 s3, v0
	v_bfe_u32 v70, v0, 4, 2
	v_and_b32_e32 v71, 15, v0
	s_lshr_b32 s3, s3, 6
	s_lshl_b32 s12, s2, 4
	s_lshl_b32 s20, s2, 11
	s_lshl_b32 s21, s3, 7
	s_lshl_b32 s22, s3, 6
	v_lshlrev_b32_e32 v72, 7, v71
	v_lshl_or_b32 v72, v70, 5, v72
	v_lshlrev_b32_e32 v73, 12, v70
	v_lshl_or_b32 v73, v71, 3, v73
	v_lshlrev_b32_e32 v74, 3, v71
	v_lshlrev_b32_e32 v75, 9, v70
	v_lshl_or_b32 v75, v71, 2, v75
	s_add_i32 s23, s22, 0x1080
	v_lshl_add_u32 v76, v70, 4, s23
	s_waitcnt lgkmcnt(0)
	s_load_dword s13, s[16:17], 0x0
	s_add_u32 s4, s4, s20
	s_addc_u32 s5, s5, 0
	s_add_u32 s8, s8, s21
	s_addc_u32 s9, s9, 0
	global_load_dwordx4 v[2:5], v72, s[4:5] nt
	global_load_dwordx4 v[6:9], v72, s[4:5] offset:16 nt
	global_load_dwordx2 v[26:27], v73, s[8:9]
	global_load_dwordx2 v[28:29], v73, s[8:9] offset:256
	global_load_dwordx2 v[30:31], v73, s[8:9] offset:512
	global_load_dwordx2 v[32:33], v73, s[8:9] offset:768
	global_load_dwordx2 v[34:35], v73, s[8:9] offset:1024
	global_load_dwordx2 v[36:37], v73, s[8:9] offset:1280
	global_load_dwordx2 v[38:39], v73, s[8:9] offset:1536
	global_load_dwordx2 v[40:41], v73, s[8:9] offset:1792
	global_load_dwordx2 v[42:43], v73, s[8:9] offset:2048
	global_load_dwordx2 v[44:45], v73, s[8:9] offset:2304
	global_load_dwordx2 v[46:47], v73, s[8:9] offset:2560
	global_load_dwordx2 v[48:49], v73, s[8:9] offset:2816
	global_load_dwordx2 v[50:51], v73, s[8:9] offset:3072
	global_load_dwordx2 v[52:53], v73, s[8:9] offset:3328
	global_load_dwordx2 v[54:55], v73, s[8:9] offset:3584
	global_load_dwordx2 v[56:57], v73, s[8:9] offset:3840
	s_add_u32 s6, s6, s20
	s_addc_u32 s7, s7, 0
	s_add_u32 s6, s6, s22
	s_addc_u32 s7, s7, 0
	global_load_dword v60, v75, s[6:7] nt
	global_load_dword v61, v75, s[6:7] offset:128 nt
	global_load_dword v62, v75, s[6:7] offset:256 nt
	global_load_dword v63, v75, s[6:7] offset:384 nt
	s_add_u32 s10, s10, s21
	s_addc_u32 s11, s11, 0
	global_load_dwordx2 v[58:59], v74, s[10:11]
	s_add_u32 s14, s14, s21
	s_addc_u32 s15, s15, 0
	global_load_dwordx2 v[68:69], v74, s[14:15]
	s_waitcnt vmcnt(22)
	v_cvt_f32_f16_e32 v10, v2
	v_max_f32_e32 v10, 0, v10
	v_cvt_f32_f16_sdwa v11, v2 dst_sel:DWORD dst_unused:UNUSED_PAD src0_sel:WORD_1
	v_max_f32_e32 v11, 0, v11
	s_waitcnt vmcnt(21)
	v_mfma_f32_16x16x4_f32 a[0:3], v10, v26, 0
	v_cvt_f32_f16_e32 v12, v3
	v_max_f32_e32 v12, 0, v12
	v_mfma_f32_16x16x4_f32 a[4:7], v10, v27, 0
	s_waitcnt vmcnt(20)
	v_mfma_f32_16x16x4_f32 a[0:3], v11, v28, a[0:3]
	v_cvt_f32_f16_sdwa v13, v3 dst_sel:DWORD dst_unused:UNUSED_PAD src0_sel:WORD_1
	v_max_f32_e32 v13, 0, v13
	v_mfma_f32_16x16x4_f32 a[4:7], v11, v29, a[4:7]
	s_waitcnt vmcnt(19)
	v_mfma_f32_16x16x4_f32 a[0:3], v12, v30, a[0:3]
	v_cvt_f32_f16_e32 v14, v4
	v_max_f32_e32 v14, 0, v14
	v_mfma_f32_16x16x4_f32 a[4:7], v12, v31, a[4:7]
	s_waitcnt vmcnt(18)
	v_mfma_f32_16x16x4_f32 a[0:3], v13, v32, a[0:3]
	v_cvt_f32_f16_sdwa v15, v4 dst_sel:DWORD dst_unused:UNUSED_PAD src0_sel:WORD_1
	v_max_f32_e32 v15, 0, v15
	v_mfma_f32_16x16x4_f32 a[4:7], v13, v33, a[4:7]
	s_waitcnt vmcnt(17)
	v_mfma_f32_16x16x4_f32 a[0:3], v14, v34, a[0:3]
	v_cvt_f32_f16_e32 v16, v5
	v_max_f32_e32 v16, 0, v16
	v_mfma_f32_16x16x4_f32 a[4:7], v14, v35, a[4:7]
	s_waitcnt vmcnt(16)
	v_mfma_f32_16x16x4_f32 a[0:3], v15, v36, a[0:3]
	v_cvt_f32_f16_sdwa v17, v5 dst_sel:DWORD dst_unused:UNUSED_PAD src0_sel:WORD_1
	v_max_f32_e32 v17, 0, v17
	v_mfma_f32_16x16x4_f32 a[4:7], v15, v37, a[4:7]
	s_waitcnt vmcnt(15)
	v_mfma_f32_16x16x4_f32 a[0:3], v16, v38, a[0:3]
	v_cvt_f32_f16_e32 v18, v6
	v_max_f32_e32 v18, 0, v18
	v_mfma_f32_16x16x4_f32 a[4:7], v16, v39, a[4:7]
	s_waitcnt vmcnt(14)
	v_mfma_f32_16x16x4_f32 a[0:3], v17, v40, a[0:3]
	v_cvt_f32_f16_sdwa v19, v6 dst_sel:DWORD dst_unused:UNUSED_PAD src0_sel:WORD_1
	v_max_f32_e32 v19, 0, v19
	v_mfma_f32_16x16x4_f32 a[4:7], v17, v41, a[4:7]
	s_waitcnt vmcnt(13)
	v_mfma_f32_16x16x4_f32 a[0:3], v18, v42, a[0:3]
	v_cvt_f32_f16_e32 v20, v7
	v_max_f32_e32 v20, 0, v20
	v_mfma_f32_16x16x4_f32 a[4:7], v18, v43, a[4:7]
	s_waitcnt vmcnt(12)
	v_mfma_f32_16x16x4_f32 a[0:3], v19, v44, a[0:3]
	v_cvt_f32_f16_sdwa v21, v7 dst_sel:DWORD dst_unused:UNUSED_PAD src0_sel:WORD_1
	v_max_f32_e32 v21, 0, v21
	v_mfma_f32_16x16x4_f32 a[4:7], v19, v45, a[4:7]
	s_waitcnt vmcnt(11)
	v_mfma_f32_16x16x4_f32 a[0:3], v20, v46, a[0:3]
	v_cvt_f32_f16_e32 v22, v8
	v_max_f32_e32 v22, 0, v22
	v_mfma_f32_16x16x4_f32 a[4:7], v20, v47, a[4:7]
	s_waitcnt vmcnt(10)
	v_mfma_f32_16x16x4_f32 a[0:3], v21, v48, a[0:3]
	v_cvt_f32_f16_sdwa v23, v8 dst_sel:DWORD dst_unused:UNUSED_PAD src0_sel:WORD_1
	v_max_f32_e32 v23, 0, v23
	v_mfma_f32_16x16x4_f32 a[4:7], v21, v49, a[4:7]
	s_waitcnt vmcnt(9)
	v_mfma_f32_16x16x4_f32 a[0:3], v22, v50, a[0:3]
	v_cvt_f32_f16_e32 v24, v9
	v_max_f32_e32 v24, 0, v24
	v_mfma_f32_16x16x4_f32 a[4:7], v22, v51, a[4:7]
	s_waitcnt vmcnt(8)
	v_mfma_f32_16x16x4_f32 a[0:3], v23, v52, a[0:3]
	v_cvt_f32_f16_sdwa v25, v9 dst_sel:DWORD dst_unused:UNUSED_PAD src0_sel:WORD_1
	v_max_f32_e32 v25, 0, v25
	v_mfma_f32_16x16x4_f32 a[4:7], v23, v53, a[4:7]
	s_waitcnt vmcnt(7)
	v_mfma_f32_16x16x4_f32 a[0:3], v24, v54, a[0:3]
	v_mfma_f32_16x16x4_f32 a[4:7], v24, v55, a[4:7]
	s_waitcnt vmcnt(6)
	v_mfma_f32_16x16x4_f32 a[0:3], v25, v56, a[0:3]
	v_mfma_f32_16x16x4_f32 a[4:7], v25, v57, a[4:7]
	v_cmp_eq_u32_e32 vcc, 0, v71
	s_waitcnt vmcnt(1)
	v_cvt_f32_f16_sdwa v64, v60 dst_sel:DWORD dst_unused:UNUSED_PAD src0_sel:WORD_1
	v_cvt_f32_f16_sdwa v65, v61 dst_sel:DWORD dst_unused:UNUSED_PAD src0_sel:WORD_1
	v_cvt_f32_f16_sdwa v66, v62 dst_sel:DWORD dst_unused:UNUSED_PAD src0_sel:WORD_1
	v_cvt_f32_f16_sdwa v67, v63 dst_sel:DWORD dst_unused:UNUSED_PAD src0_sel:WORD_1
	v_cvt_f32_f16_e32 v60, v60
	v_cvt_f32_f16_e32 v61, v61
	v_cvt_f32_f16_e32 v62, v62
	v_cvt_f32_f16_e32 v63, v63
	v_add_f32_e32 v60, v58, v60
	v_add_f32_e32 v64, v59, v64
	v_add_f32_e32 v61, v58, v61
	v_add_f32_e32 v65, v59, v65
	v_add_f32_e32 v62, v58, v62
	v_add_f32_e32 v66, v59, v66
	v_add_f32_e32 v63, v58, v63
	v_add_f32_e32 v67, v59, v67
	s_nop 1
	v_accvgpr_read_b32 v2, a0
	v_accvgpr_read_b32 v3, a1
	v_accvgpr_read_b32 v4, a2
	v_accvgpr_read_b32 v5, a3
	v_accvgpr_read_b32 v6, a4
	v_accvgpr_read_b32 v7, a5
	v_accvgpr_read_b32 v8, a6
	v_accvgpr_read_b32 v9, a7
	v_add_f32_e32 v2, v2, v60
	v_add_f32_e32 v3, v3, v61
	v_add_f32_e32 v4, v4, v62
	v_add_f32_e32 v5, v5, v63
	v_add_f32_e32 v6, v6, v64
	v_add_f32_e32 v7, v7, v65
	v_add_f32_e32 v8, v8, v66
	v_add_f32_e32 v9, v9, v67
	v_max_f32_e32 v2, 0, v2
	v_max_f32_e32 v3, 0, v3
	v_max_f32_e32 v4, 0, v4
	v_max_f32_e32 v5, 0, v5
	v_max_f32_e32 v6, 0, v6
	v_max_f32_e32 v7, 0, v7
	v_max_f32_e32 v8, 0, v8
	v_max_f32_e32 v9, 0, v9
	s_waitcnt vmcnt(0)
	v_mul_f32_e32 v6, v69, v6
	v_mul_f32_e32 v7, v69, v7
	v_mul_f32_e32 v8, v69, v8
	v_mul_f32_e32 v9, v69, v9
	v_fmac_f32_e32 v6, v68, v2
	v_fmac_f32_e32 v7, v68, v3
	v_fmac_f32_e32 v8, v68, v4
	v_fmac_f32_e32 v9, v68, v5
	v_add_f32_dpp v6, v6, v6 quad_perm:[1,0,3,2] row_mask:0xf bank_mask:0xf
	v_add_f32_dpp v7, v7, v7 quad_perm:[1,0,3,2] row_mask:0xf bank_mask:0xf
	v_add_f32_dpp v8, v8, v8 quad_perm:[1,0,3,2] row_mask:0xf bank_mask:0xf
	v_add_f32_dpp v9, v9, v9 quad_perm:[1,0,3,2] row_mask:0xf bank_mask:0xf
	v_add_f32_dpp v6, v6, v6 quad_perm:[2,3,0,1] row_mask:0xf bank_mask:0xf
	v_add_f32_dpp v7, v7, v7 quad_perm:[2,3,0,1] row_mask:0xf bank_mask:0xf
	v_add_f32_dpp v8, v8, v8 quad_perm:[2,3,0,1] row_mask:0xf bank_mask:0xf
	v_add_f32_dpp v9, v9, v9 quad_perm:[2,3,0,1] row_mask:0xf bank_mask:0xf
	v_add_f32_dpp v6, v6, v6 row_half_mirror row_mask:0xf bank_mask:0xf
	v_add_f32_dpp v7, v7, v7 row_half_mirror row_mask:0xf bank_mask:0xf
	v_add_f32_dpp v8, v8, v8 row_half_mirror row_mask:0xf bank_mask:0xf
	v_add_f32_dpp v9, v9, v9 row_half_mirror row_mask:0xf bank_mask:0xf
	v_add_f32_dpp v6, v6, v6 row_mirror row_mask:0xf bank_mask:0xf
	v_add_f32_dpp v7, v7, v7 row_mirror row_mask:0xf bank_mask:0xf
	v_add_f32_dpp v8, v8, v8 row_mirror row_mask:0xf bank_mask:0xf
	v_add_f32_dpp v9, v9, v9 row_mirror row_mask:0xf bank_mask:0xf
	s_and_saveexec_b64 s[2:3], vcc
	ds_write_b128 v76, v[6:9]
	s_or_b64 exec, exec, s[2:3]
	v_cmp_gt_u32_e32 vcc, 16, v0
	s_waitcnt lgkmcnt(0)
	s_barrier
	s_and_saveexec_b64 s[2:3], vcc
	s_cbranch_execz .Lfinal_done
	v_lshlrev_b32_e32 v1, 2, v0
	v_add_u32_e32 v1, 0x1000, v1
	ds_read2_b32 v[2:3], v1 offset0:32 offset1:48
	v_or_b32_e32 v0, s12, v0
	v_ashrrev_i32_e32 v1, 31, v0
	v_lshl_add_u64 v[0:1], v[0:1], 2, s[18:19]
	s_waitcnt lgkmcnt(0)
	v_add_f32_e32 v2, v2, v3
	v_add_f32_e32 v2, s13, v2
	global_store_dword v[0:1], v2, off
